# gdnout2: the lane's eight gdn_norm_w pieces (loop-invariant) loaded once in front of the unit loop; the per-unit reloads (two per wait) become register copies (2 wait states behind the 128-bit stores
# speedup vs baseline: 1.0071x; 1.0052x over previous
; #define LAS __attribute__((address_space(3)))
; DI int tidx() { int t = threadIdx.x & 255; asm volatile("" : "+v"(t)); return t; }
; DI void gdn_out_unit(const Params& p, int U, char* lds) {
;   const int tid = tidx(), lane = tid & 63, wv = tid >> 6, r32 = lane & 31, hi = lane >> 5;
;   const int b = U >> 9, h = (U >> 7) & 3, c = U & 127;
;   bf16_t* proj = (bf16_t*)(p.ws + WS_P);
;   const char* wfg = (const char*)(p.ws + WS_WF) + (size_t)U * 16384 + lane * 16;
;   const char* qfg = (const char*)p.out + (size_t)U * 16384 + lane * 16;
;   const char* afg = (const char*)p.out + 64 * MiB + (size_t)U * 8192 + lane * 16;
;   const bf16_t* UF = (const bf16_t*)(p.ws + WS_UF) + (size_t)U * 8192;
;   const bf16x8* SC = (const bf16x8*)(p.ws + WS_SC + (size_t)U * 32768 + (size_t)wv * 8192) + lane;
;   bf16_t* ol = (bf16_t*)(lds + 40960);
;   __syncthreads();
; #pragma unroll
;   for (int i = 0; i < 4; ++i) {
;     __builtin_amdgcn_global_load_lds((const unsigned*)(wfg + (4 * wv + i) * 1024), (LAS unsigned*)(lds + (4 * wv + i) * 1024), 16, 0, 0);
;     __builtin_amdgcn_global_load_lds((const unsigned*)(qfg + (4 * wv + i) * 1024), (LAS unsigned*)(lds + 16384 + (4 * wv + i) * 1024), 16, 0, 0);
;   }
; #pragma unroll
;   for (int i = 0; i < 2; ++i) __builtin_amdgcn_global_load_lds((const unsigned*)(afg + (2 * wv + i) * 1024), (LAS unsigned*)(lds + 32768 + (2 * wv + i) * 1024), 16, 0, 0);
;   bf16x8 Sb[4][2];
; #pragma unroll
;   for (int m = 0; m < 4; ++m) { Sb[m][0] = SC[(m * 2 + 0) * 64]; Sb[m][1] = SC[(m * 2 + 1) * 64]; }
;   u32x4 uu[4];
; #pragma unroll
;   for (int i2 = 0; i2 < 2; ++i2) { uu[2 * i2] = *(const u32x4*)(UF + (size_t)((i2 * 4 + wv) * 64 + lane) * 16); uu[2 * i2 + 1] = *(const u32x4*)(UF + (size_t)((i2 * 4 + wv) * 64 + lane) * 16 + 8); }
;   __syncthreads();
; DI void phase_gdnout2(const Params& p, int bid, int nb, char* lds) {
;   for (int U = bid; U < 2048; U += nb) gdn_out_unit(p, U, lds);
.LBB0_1334:
	s_or_b64 exec, exec, s[0:1]
	v_ashrrev_i32_e32 v177, 31, v176
	s_waitcnt lgkmcnt(0)
	s_barrier
	s_and_saveexec_b64 s[0:1], s[4:5]
	s_cbranch_execz .LBB0_1337
	v_readlane_b32 s2, v250, 0
	v_lshlrev_b64 v[0:1], 13, v[176:177]
	v_readlane_b32 s3, v250, 1
	s_ashr_i32 s91, s90, 31
	v_lshl_add_u64 v[0:1], s[66:67], 0, v[0:1]
	s_mov_b64 s[6:7], 0x4000400
	s_movk_i32 s34, 0xfc00
	v_lshl_add_u32 v88, s2, 7, v189
	s_lshl_b32 s2, s86, 7
	s_waitcnt vmcnt(9)
	v_lshlrev_b64 v[76:77], 15, v[176:177]
	s_lshl_b64 s[4:5], s[90:91], 15
	s_waitcnt vmcnt(8)
	v_lshl_add_u64 v[78:79], v[0:1], 0, s[6:7]
	s_lshl_b64 s[6:7], s[90:91], 13
	v_lshlrev_b64 v[80:81], 14, v[176:177]
	s_lshl_b64 s[8:9], s[90:91], 14
	s_mov_b64 s[10:11], 0
	s_mov_b64 s[12:13], 0x1e000000
	s_mov_b64 s[14:15], 0x1e000400
	s_mov_b64 s[16:17], 0x400
	s_mov_b64 s[24:25], 0x1e000800
	s_mov_b64 s[26:27], 0x800
	s_mov_b64 s[28:29], 0x1e000c00
	s_mov_b64 s[30:31], 0xc00
	s_mov_b32 s35, -1
	s_brev_b32 s3, 64
	s_mov_b32 s18, 0x2001000
	s_mov_b64 s[38:39], 0x1c000000
	s_brev_b32 s19, 56
	s_movk_i32 s22, 0xffc0
	s_movk_i32 s23, 0x1fc0
	s_movk_i32 s42, 0x2c00
	v_mov_b64_e32 v[82:83], s[58:59]
	v_mov_b32_e32 v85, 0
	s_movk_i32 s43, 0x110
	s_mov_b64 s[40:41], 0x1800
	s_movk_i32 s44, 0x1000
	v_mov_b32_e32 v89, 0x358637bd
	s_mov_b32 s45, 0x800000
	s_movk_i32 s48, 0x7ff
	v_mov_b32_e32 v90, v176
	v_and_b32_e32 v245, 3, v206
	v_lshlrev_b32_e32 v245, 7, v245
	global_load_dwordx4 v[212:215], v245, s[76:77]
	global_load_dwordx4 v[216:219], v245, s[76:77] offset:16
	global_load_dwordx4 v[220:223], v245, s[76:77] offset:32
	global_load_dwordx4 v[224:227], v245, s[76:77] offset:48
	global_load_dwordx4 v[228:231], v245, s[76:77] offset:64
	global_load_dwordx4 v[232:235], v245, s[76:77] offset:80
	global_load_dwordx4 v[236:239], v245, s[76:77] offset:96
	global_load_dwordx4 v[240:243], v245, s[76:77] offset:112
.LBB0_1336:
	v_mov_b32_e32 v86, v206
	s_nop 0
	v_ashrrev_i32_e32 v0, 6, v86
	v_ashrrev_i32_e32 v87, 31, v86
	v_lshlrev_b32_e32 v1, 4, v86
	v_add_u32_e32 v2, 0x100, v86
	v_lshlrev_b32_e32 v8, 12, v0
	v_lshlrev_b64 v[4:5], 5, v[86:87]
	v_and_b32_e32 v10, 0x3f0, v1
	v_ashrrev_i32_e32 v3, 31, v2
	v_add_u32_e32 v12, v146, v8
	v_lshl_add_u64 v[4:5], v[80:81], 0, v[4:5]
	v_ashrrev_i32_e32 v1, 31, v0
	v_lshlrev_b32_e32 v11, 11, v0
	v_ashrrev_i32_e32 v7, 31, v8
	v_or_b32_e32 v6, v8, v10
	v_lshlrev_b64 v[2:3], 5, v[2:3]
	v_add_u32_e32 v16, 0x4400, v12
	v_add_u32_e32 v17, 0x800, v12
	v_lshl_add_u64 v[4:5], s[84:85], 0, v[4:5]
	v_lshlrev_b64 v[0:1], 13, v[0:1]
	v_ashrrev_i32_e32 v9, 31, v11
	v_or_b32_e32 v8, v11, v10
	v_add_u32_e32 v11, v146, v11
	v_lshl_add_u64 v[6:7], v[80:81], 0, v[6:7]
	v_lshl_add_u64 v[2:3], v[80:81], 0, v[2:3]
	v_readfirstlane_b32 s60, v16
	v_readfirstlane_b32 s61, v17
	v_lshl_add_u64 v[16:17], v[4:5], 0, s[38:39]
	v_add_co_u32_e32 v4, vcc, s19, v4
	v_add_u32_e32 v87, v146, v10
	v_or_b32_e32 v0, v0, v10
	v_readfirstlane_b32 s49, v12
	v_add_u32_e32 v14, 0x4000, v12
	v_add_u32_e32 v15, 0x400, v12
	v_add_u32_e32 v18, 0x4800, v12
	v_add_u32_e32 v19, 0xc00, v12
	v_add_u32_e32 v20, 0x4c00, v12
	v_add_u32_e32 v21, 0x8000, v11
	v_add_u32_e32 v22, 0x8400, v11
	v_lshl_add_u64 v[10:11], s[84:85], 0, v[6:7]
	v_lshl_add_u64 v[12:13], s[66:67], 0, v[6:7]
	v_addc_co_u32_e32 v5, vcc, 0, v5, vcc
	v_lshl_add_u64 v[6:7], s[84:85], 0, v[2:3]
	v_lshl_add_u64 v[0:1], v[76:77], 0, v[0:1]
	v_add_co_u32_e32 v36, vcc, s19, v6
	v_readfirstlane_b32 s68, v18
	v_readfirstlane_b32 s69, v19
	v_readfirstlane_b32 s70, v20
	v_readfirstlane_b32 s71, v21
	v_lshl_add_u64 v[18:19], s[84:85], 0, v[0:1]
	v_lshl_add_u64 v[20:21], v[10:11], 0, s[12:13]
	v_addc_co_u32_e32 v37, vcc, 0, v7, vcc
	s_mov_b32 m0, s49
	s_barrier
	global_load_lds_dwordx4 v[20:21], off
	v_add_co_u32_e32 v20, vcc, s3, v18
	global_load_dwordx4 v[0:3], v[4:5], off
	s_nop 0
	v_addc_co_u32_e32 v21, vcc, 0, v19, vcc
	v_add_co_u32_e32 v18, vcc, s18, v18
	v_lshl_add_u64 v[4:5], v[6:7], 0, s[38:39]
	s_nop 0
	v_addc_co_u32_e32 v19, vcc, 0, v19, vcc
	global_load_dwordx4 v[4:7], v[4:5], off offset:16
	s_nop 0
	global_load_dwordx4 v[92:95], v[18:19], off offset:-4096
	global_load_dwordx4 v[32:35], v[16:17], off offset:16
	s_nop 0
	global_load_dwordx4 v[36:39], v[36:37], off
	s_nop 0
	global_load_dwordx4 v[96:99], v[20:21], off offset:3072
	v_readfirstlane_b32 s50, v14
	s_mov_b32 m0, s50
	v_readfirstlane_b32 s51, v15
	global_load_lds_dwordx4 v[12:13], off
	global_load_dwordx4 v[100:103], v[20:21], off offset:1024
	global_load_dwordx4 v[104:107], v[20:21], off offset:2048
	global_load_dwordx4 v[108:111], v[18:19], off
	global_load_dwordx4 v[72:75], v[18:19], off offset:1024
	global_load_dwordx4 v[68:71], v[18:19], off offset:2048
	global_load_dwordx4 v[64:67], v[18:19], off offset:3072
	v_readfirstlane_b32 s72, v22
	v_lshl_add_u64 v[22:23], v[10:11], 0, s[14:15]
	s_mov_b32 m0, s51
	v_lshl_add_u64 v[24:25], v[12:13], 0, s[16:17]
	global_load_lds_dwordx4 v[22:23], off
	s_mov_b32 m0, s60
	v_lshl_add_u64 v[26:27], v[10:11], 0, s[24:25]
	global_load_lds_dwordx4 v[24:25], off
	s_mov_b32 m0, s61
	v_lshl_add_u64 v[28:29], v[12:13], 0, s[26:27]
	global_load_lds_dwordx4 v[26:27], off
	s_mov_b32 m0, s68
	v_lshl_add_u64 v[10:11], v[10:11], 0, s[28:29]
	global_load_lds_dwordx4 v[28:29], off
	s_mov_b32 m0, s69
	v_lshl_add_u64 v[8:9], v[78:79], 0, v[8:9]
	v_lshl_add_u64 v[30:31], v[12:13], 0, s[30:31]
	global_load_lds_dwordx4 v[10:11], off
	s_mov_b32 m0, s70
	v_lshl_add_u64 v[14:15], v[8:9], 0, s[34:35]
	global_load_lds_dwordx4 v[30:31], off
	s_mov_b32 m0, s71
	v_and_b32_e32 v91, 31, v86
	global_load_lds_dwordx4 v[14:15], off
	s_mov_b32 m0, s72
	v_and_b32_e32 v84, 0x180, v90
	global_load_lds_dwordx4 v[8:9], off
	s_waitcnt vmcnt(0) lgkmcnt(0)
	s_barrier
; DI float bflo(unsigned u) { return __uint_as_float(u << 16); }
; DI float bfhi(unsigned u) { return __uint_as_float(u & 0xffff0000u); }
; #define MFMA32(a, b, c) __builtin_amdgcn_mfma_f32_32x32x16_bf16((a), (b), (c), 0, 0, 0)
; DI bf16x8 packS(const f32x16& x, int s) { return pack8(x[8 * s], x[8 * s + 1], x[8 * s + 2], x[8 * s + 3], x[8 * s + 4], x[8 * s + 5], x[8 * s + 6], x[8 * s + 7]); }
; DI void gdn_out_unit(const Params& p, int U, char* lds) {
;     ...
;   const char* lw = lds + lane * 16; const char* lq = lds + 16384 + lane * 16; const char* la = lds + 32768 + lane * 16;
;   f32x16 vn[2], o[2];
; #pragma unroll
;   for (int i2 = 0; i2 < 2; ++i2) {
; #pragma unroll
;     for (int e = 0; e < 4; ++e) { vn[i2][2 * e] = bflo(uu[2 * i2][e]); vn[i2][2 * e + 1] = bfhi(uu[2 * i2][e]); vn[i2][8 + 2 * e] = bflo(uu[2 * i2 + 1][e]); vn[i2][8 + 2 * e + 1] = bfhi(uu[2 * i2 + 1][e]); }
; #pragma unroll
;     for (int r = 0; r < 16; ++r) o[i2][r] = 0.f;
; #pragma unroll
;     for (int m = 0; m < 4; ++m)
; #pragma unroll
;       for (int s = 0; s < 2; ++s) {
;         vn[i2] = MFMA32(*(const bf16x8*)(lw + ((i2 * 4 + m) * 2 + s) * 1024), Sb[m][s], vn[i2]);
;         o[i2] = MFMA32(*(const bf16x8*)(lq + ((i2 * 4 + m) * 2 + s) * 1024), Sb[m][s], o[i2]);
;       }
;   }
;   bf16x8 Vb[2][2];
; #pragma unroll
;   for (int j2 = 0; j2 < 2; ++j2) { Vb[j2][0] = packS(vn[j2], 0); Vb[j2][1] = packS(vn[j2], 1); }
	ds_read_b128 v[112:115], v87
	ds_read_b128 v[116:119], v87 offset:1024
	ds_read_b128 v[8:11], v87 offset:16384
	ds_read_b128 v[120:123], v87 offset:17408
	ds_read_b128 v[124:127], v87 offset:8192
	ds_read_b128 v[128:131], v87 offset:9216
	ds_read_b128 v[12:15], v87 offset:24576
	ds_read_b128 v[132:135], v87 offset:25600
	s_waitcnt lgkmcnt(5)
	v_mfma_f32_32x32x16_bf16 v[16:31], v[8:11], v[92:95], 0
	v_lshlrev_b32_e32 v48, 16, v0
	v_and_b32_e32 v49, 0xffff0000, v0
	v_lshlrev_b32_e32 v50, 16, v1
	v_and_b32_e32 v51, 0xffff0000, v1
	v_lshlrev_b32_e32 v52, 16, v2
	v_and_b32_e32 v53, 0xffff0000, v2
	v_lshlrev_b32_e32 v54, 16, v3
	v_and_b32_e32 v55, 0xffff0000, v3
	v_lshlrev_b32_e32 v40, 16, v4
	v_and_b32_e32 v41, 0xffff0000, v4
	v_lshlrev_b32_e32 v42, 16, v5
	v_and_b32_e32 v43, 0xffff0000, v5
	v_lshlrev_b32_e32 v44, 16, v6
	v_and_b32_e32 v45, 0xffff0000, v6
	v_lshlrev_b32_e32 v46, 16, v7
	v_and_b32_e32 v47, 0xffff0000, v7
	v_lshlrev_b32_e32 v56, 16, v32
	v_and_b32_e32 v57, 0xffff0000, v32
	v_lshlrev_b32_e32 v58, 16, v33
	v_and_b32_e32 v59, 0xffff0000, v33
	v_lshlrev_b32_e32 v60, 16, v34
	v_and_b32_e32 v61, 0xffff0000, v34
	v_lshlrev_b32_e32 v62, 16, v35
	v_and_b32_e32 v63, 0xffff0000, v35
	v_lshlrev_b32_e32 v32, 16, v36
	v_and_b32_e32 v33, 0xffff0000, v36
	v_lshlrev_b32_e32 v34, 16, v37
	v_and_b32_e32 v35, 0xffff0000, v37
	v_lshlrev_b32_e32 v36, 16, v38
	v_and_b32_e32 v37, 0xffff0000, v38
	v_lshlrev_b32_e32 v38, 16, v39
	v_and_b32_e32 v39, 0xffff0000, v39
	s_waitcnt lgkmcnt(1)
	v_mfma_f32_32x32x16_bf16 v[0:15], v[12:15], v[92:95], 0
	v_lshlrev_b32_e32 v84, 1, v84
	v_lshl_add_u64 v[78:79], v[78:79], 0, s[6:7]
	v_lshl_add_u64 v[80:81], v[80:81], 0, s[8:9]
	v_lshl_add_u64 v[76:77], v[76:77], 0, s[4:5]
	v_mfma_f32_32x32x16_bf16 v[48:63], v[112:115], v[92:95], v[48:63]
	v_mfma_f32_32x32x16_bf16 v[32:47], v[124:127], v[92:95], v[32:47]
	v_mfma_f32_32x32x16_bf16 v[16:31], v[120:123], v[100:103], v[16:31]
	s_waitcnt lgkmcnt(0)
	v_mfma_f32_32x32x16_bf16 v[0:15], v[132:135], v[100:103], v[0:15]
	v_mfma_f32_32x32x16_bf16 v[48:63], v[116:119], v[100:103], v[48:63]
	v_mfma_f32_32x32x16_bf16 v[32:47], v[128:131], v[100:103], v[32:47]
	ds_read_b128 v[92:95], v87 offset:18432
	ds_read_b128 v[100:103], v87 offset:19456
	s_waitcnt lgkmcnt(1)
	v_mfma_f32_32x32x16_bf16 v[16:31], v[92:95], v[104:107], v[16:31]
	ds_read_b128 v[92:95], v87 offset:26624
	ds_read_b128 v[112:115], v87 offset:27648
	s_waitcnt lgkmcnt(1)
	v_mfma_f32_32x32x16_bf16 v[0:15], v[92:95], v[104:107], v[0:15]
	ds_read_b128 v[92:95], v87 offset:2048
	ds_read_b128 v[116:119], v87 offset:3072
	s_waitcnt lgkmcnt(1)
	v_mfma_f32_32x32x16_bf16 v[48:63], v[92:95], v[104:107], v[48:63]
	ds_read_b128 v[92:95], v87 offset:10240
	ds_read_b128 v[120:123], v87 offset:11264
	s_waitcnt lgkmcnt(1)
	v_mfma_f32_32x32x16_bf16 v[32:47], v[92:95], v[104:107], v[32:47]
	v_mfma_f32_32x32x16_bf16 v[16:31], v[100:103], v[96:99], v[16:31]
	v_mfma_f32_32x32x16_bf16 v[0:15], v[112:115], v[96:99], v[0:15]
	v_mfma_f32_32x32x16_bf16 v[48:63], v[116:119], v[96:99], v[48:63]
	s_waitcnt lgkmcnt(0)
	v_mfma_f32_32x32x16_bf16 v[32:47], v[120:123], v[96:99], v[32:47]
	ds_read_b128 v[92:95], v87 offset:20480
	ds_read_b128 v[96:99], v87 offset:21504
	s_waitcnt lgkmcnt(1)
	v_mfma_f32_32x32x16_bf16 v[16:31], v[92:95], v[108:111], v[16:31]
	ds_read_b128 v[92:95], v87 offset:28672
	ds_read_b128 v[100:103], v87 offset:29696
	s_waitcnt lgkmcnt(1)
	v_mfma_f32_32x32x16_bf16 v[0:15], v[92:95], v[108:111], v[0:15]
	ds_read_b128 v[92:95], v87 offset:4096
	ds_read_b128 v[104:107], v87 offset:5120
	s_waitcnt lgkmcnt(1)
	v_mfma_f32_32x32x16_bf16 v[48:63], v[92:95], v[108:111], v[48:63]
	ds_read_b128 v[92:95], v87 offset:12288
	ds_read_b128 v[112:115], v87 offset:13312
	s_waitcnt lgkmcnt(1)
	v_mfma_f32_32x32x16_bf16 v[32:47], v[92:95], v[108:111], v[32:47]
	v_ashrrev_i32_e32 v108, 9, v90
	v_ashrrev_i32_e32 v109, 31, v108
	v_lshrrev_b32_e32 v110, 3, v86
	v_add_u32_e32 v90, s90, v90
	v_mfma_f32_32x32x16_bf16 v[16:31], v[96:99], v[72:75], v[16:31]
	v_mfma_f32_32x32x16_bf16 v[0:15], v[100:103], v[72:75], v[0:15]
	v_mfma_f32_32x32x16_bf16 v[48:63], v[104:107], v[72:75], v[48:63]
	s_waitcnt lgkmcnt(0)
	v_mfma_f32_32x32x16_bf16 v[32:47], v[112:115], v[72:75], v[32:47]
	ds_read_b128 v[72:75], v87 offset:22528
	ds_read_b128 v[92:95], v87 offset:23552
	s_waitcnt lgkmcnt(1)
	v_mfma_f32_32x32x16_bf16 v[16:31], v[72:75], v[68:71], v[16:31]
	ds_read_b128 v[72:75], v87 offset:30720
	ds_read_b128 v[96:99], v87 offset:31744
	s_waitcnt lgkmcnt(1)
	v_mfma_f32_32x32x16_bf16 v[0:15], v[72:75], v[68:71], v[0:15]
	ds_read_b128 v[72:75], v87 offset:6144
	ds_read_b128 v[100:103], v87 offset:7168
	s_waitcnt lgkmcnt(1)
	v_mfma_f32_32x32x16_bf16 v[48:63], v[72:75], v[68:71], v[48:63]
	ds_read_b128 v[72:75], v87 offset:14336
	ds_read_b128 v[104:107], v87 offset:15360
	s_waitcnt lgkmcnt(1)
	v_mfma_f32_32x32x16_bf16 v[32:47], v[72:75], v[68:71], v[32:47]
	v_lshlrev_b64 v[68:69], 13, v[108:109]
	v_ashrrev_i32_e32 v70, 2, v86
	v_lshlrev_b32_e32 v72, 5, v86
	v_and_b32_e32 v73, 4, v110
	v_and_or_b32 v68, v88, s23, v68
	v_ashrrev_i32_e32 v71, 31, v70
	v_and_b32_e32 v75, 0x60, v72
	v_mfma_f32_32x32x16_bf16 v[48:63], v[100:103], v[64:67], v[48:63]
	v_mul_u32_u24_e32 v72, 0x88, v73
	v_lshl_add_u64 v[68:69], v[68:69], 0, v[70:71]
	v_lshlrev_b32_e32 v74, 1, v91
	v_lshlrev_b32_e32 v71, 1, v72
	v_mad_u64_u32 v[72:73], s[50:51], v68, s42, v[82:83]
	v_and_or_b32 v74, v86, s22, v74
	v_mfma_f32_32x32x16_bf16 v[16:31], v[92:95], v[64:67], v[16:31]
	v_mad_i32_i24 v73, v69, s42, v73
	v_mul_lo_u32 v91, v70, s43
	v_lshlrev_b32_e32 v70, 2, v75
	v_add3_u32 v86, v146, v74, v71
	v_add3_u32 v71, v146, v71, v74
	v_lshl_add_u64 v[68:69], v[72:73], 0, v[84:85]
	v_lshlrev_b32_e32 v84, 1, v75
	v_mfma_f32_32x32x16_bf16 v[0:15], v[96:99], v[64:67], v[0:15]
	v_cvt_pk_bf16_f32 v48, v48, v49
	v_cvt_pk_bf16_f32 v49, v50, v51
	v_cvt_pk_bf16_f32 v50, v52, v53
	v_cvt_pk_bf16_f32 v51, v54, v55
	v_lshl_add_u64 v[68:69], v[68:69], 0, v[84:85]
	v_add_co_u32_e32 v102, vcc, s44, v68
	s_waitcnt lgkmcnt(0)
; DI bf16_t f2bf(float x) { return (bf16_t)(pk2(x, 0.f) & 0xffffu); }
; DI void gdn_out_unit(const Params& p, int U, char* lds) {
;     ...
;   bf16x8 Vb[2][2];
; #pragma unroll
;   for (int j2 = 0; j2 < 2; ++j2) { Vb[j2][0] = packS(vn[j2], 0); Vb[j2][1] = packS(vn[j2], 1); }
; #pragma unroll
;   for (int i2 = 0; i2 < 2; ++i2)
; #pragma unroll
;     for (int j2 = 0; j2 <= i2; ++j2)
; #pragma unroll
;       for (int s = 0; s < 2; ++s) o[i2] = MFMA32(*(const bf16x8*)(la + ((i2 * 2 + j2) * 2 + s) * 1024), Vb[j2][s], o[i2]);
;   __syncthreads();
; #pragma unroll
;   for (int i2 = 0; i2 < 2; ++i2)
; #pragma unroll
;     for (int r = 0; r < 16; ++r) ol[(32 * i2 + crow(r, hi)) * 136 + 32 * wv + r32] = f2bf(o[i2][r]);
;   __syncthreads();
;   {
;     const size_t t0 = (size_t)b * S_ + c * 64;
;     const int row = tid >> 2, q4 = tid & 3;
;     const bf16_t* gzp = proj + (t0 + row) * PP + 3072 + h * 128 + 32 * q4;
;     bf16_t* op = proj + (t0 + row) * PP + 1536 + h * 128 + 32 * q4;
;     float ss = 0.f;
; #pragma unroll
;     for (int q = 0; q < 4; ++q) { const u32x4 w = *(const u32x4*)(ol + row * 136 + 32 * q4 + 8 * q);
; #pragma unroll
;       for (int e = 0; e < 4; ++e) { const float a0 = bflo(w[e]), a1 = bfhi(w[e]); ss += a0 * a0 + a1 * a1; } }
;     ss += __uint_as_float((unsigned)__builtin_amdgcn_update_dpp(0, (int)__float_as_uint(ss), 0xB1, 0xF, 0xF, true));
;     ss += __uint_as_float((unsigned)__builtin_amdgcn_update_dpp(0, (int)__float_as_uint(ss), 0x4E, 0xF, 0xF, true));
;     const float rstd = rsqrtf(ss * (1.f / 128.f) + 1e-6f);
; #pragma unroll
;     for (int q = 0; q < 4; ++q) {
;       const u32x4 w = *(const u32x4*)(ol + row * 136 + 32 * q4 + 8 * q), gz = *(const u32x4*)(gzp + 8 * q);
;       const f32x4 n0 = *(const f32x4*)(p.gdn_norm_w + 32 * q4 + 8 * q), n1 = *(const f32x4*)(p.gdn_norm_w + 32 * q4 + 8 * q + 4);
;       float y[8];
; #pragma unroll
;       for (int e = 0; e < 4; ++e) { const float z0 = bflo(gz[e]), z1 = bfhi(gz[e]);
;         const float g0 = (2 * e < 4) ? n0[(2 * e) & 3] : n1[(2 * e) & 3], g1 = (2 * e + 1 < 4) ? n0[(2 * e + 1) & 3] : n1[(2 * e + 1) & 3];
;         y[2 * e] = bflo(w[e]) * rstd * g0 * (z0 * sigmoidf_(z0));
;         y[2 * e + 1] = bfhi(w[e]) * rstd * g1 * (z1 * sigmoidf_(z1)); }
;       u32x4 wv4 = {pk2(y[0], y[1]), pk2(y[2], y[3]), pk2(y[4], y[5]), pk2(y[6], y[7])};
;       *(u32x4*)(op + 8 * q) = wv4;
	v_mfma_f32_32x32x16_bf16 v[32:47], v[104:107], v[64:67], v[32:47]
	ds_read_b128 v[64:67], v87 offset:32768
	ds_read_b128 v[72:75], v87 offset:33792
	v_add3_u32 v91, v146, v91, v84
	v_addc_co_u32_e32 v103, vcc, 0, v69, vcc
	v_lshl_add_u64 v[100:101], v[68:69], 0, s[40:41]
	v_add_u32_e32 v88, s2, v88
	s_nop 5
	v_cvt_pk_bf16_f32 v32, v32, v33
	s_waitcnt lgkmcnt(1)
	v_mfma_f32_32x32x16_bf16 v[16:31], v[64:67], v[48:51], v[16:31]
	ds_read_b128 v[52:55], v87 offset:36864
	ds_read_b128 v[64:67], v87 offset:37888
	ds_read_b128 v[92:95], v87 offset:38912
	ds_read_b128 v[96:99], v87 offset:39936
	v_cvt_pk_bf16_f32 v33, v34, v35
	v_cvt_pk_bf16_f32 v34, v36, v37
	v_cvt_pk_bf16_f32 v35, v38, v39
	v_cvt_pk_bf16_f32 v36, v40, v41
	v_cvt_pk_bf16_f32 v37, v42, v43
	v_cvt_pk_bf16_f32 v38, v44, v45
	s_waitcnt lgkmcnt(3)
	v_mfma_f32_32x32x16_bf16 v[0:15], v[52:55], v[48:51], v[0:15]
	v_cvt_pk_bf16_f32 v48, v56, v57
	v_cvt_pk_bf16_f32 v49, v58, v59
	v_cvt_pk_bf16_f32 v50, v60, v61
	v_cvt_pk_bf16_f32 v51, v62, v63
	v_cvt_pk_bf16_f32 v39, v46, v47
	s_waitcnt lgkmcnt(0)
	s_barrier
	v_mfma_f32_32x32x16_bf16 v[0:15], v[64:67], v[48:51], v[0:15]
	v_mfma_f32_32x32x16_bf16 v[0:15], v[92:95], v[32:35], v[0:15]
	v_mfma_f32_32x32x16_bf16 v[16:31], v[72:75], v[48:51], v[16:31]
	v_mfma_f32_32x32x16_bf16 v[0:15], v[96:99], v[36:39], v[0:15]
	s_nop 10
	v_cvt_pk_bf16_f32 v16, v16, s0
	v_cvt_pk_bf16_f32 v17, v17, s0
	v_cvt_pk_bf16_f32 v18, v18, s0
	v_cvt_pk_bf16_f32 v19, v19, s0
	v_cvt_pk_bf16_f32 v20, v20, s0
	v_cvt_pk_bf16_f32 v21, v21, s0
	v_cvt_pk_bf16_f32 v22, v22, s0
	v_cvt_pk_bf16_f32 v23, v23, s0
	v_cvt_pk_bf16_f32 v26, v26, s0
	v_cvt_pk_bf16_f32 v27, v27, s0
	v_cvt_pk_bf16_f32 v28, v28, s0
	v_cvt_pk_bf16_f32 v29, v29, s0
	v_cvt_pk_bf16_f32 v0, v0, s0
	v_cvt_pk_bf16_f32 v1, v1, s0
	v_cvt_pk_bf16_f32 v2, v2, s0
	v_cvt_pk_bf16_f32 v3, v3, s0
	v_cvt_pk_bf16_f32 v4, v4, s0
	v_cvt_pk_bf16_f32 v5, v5, s0
	v_cvt_pk_bf16_f32 v6, v6, s0
	v_cvt_pk_bf16_f32 v7, v7, s0
	v_cvt_pk_bf16_f32 v8, v8, s0
	v_cvt_pk_bf16_f32 v9, v9, s0
	v_cvt_pk_bf16_f32 v10, v10, s0
	v_cvt_pk_bf16_f32 v11, v11, s0
	v_cvt_pk_bf16_f32 v12, v12, s0
	v_cvt_pk_bf16_f32 v13, v13, s0
	v_cvt_pk_bf16_f32 v14, v14, s0
	v_cvt_pk_bf16_f32 v15, v15, s0
	v_cvt_pk_bf16_f32 v24, v24, s0
	v_cvt_pk_bf16_f32 v25, v25, s0
	v_cvt_pk_bf16_f32 v30, v30, s0
	v_cvt_pk_bf16_f32 v31, v31, s0
	ds_write_b16 v86, v16 offset:40960
	ds_write_b16 v71, v17 offset:41232
	ds_write_b16 v71, v18 offset:41504
	ds_write_b16 v71, v19 offset:41776
	ds_write_b16 v71, v20 offset:43136
	ds_write_b16 v71, v21 offset:43408
	ds_write_b16 v71, v22 offset:43680
	ds_write_b16 v71, v23 offset:43952
	ds_write_b16 v71, v24 offset:45312
	ds_write_b16 v71, v25 offset:45584
	ds_write_b16 v71, v26 offset:45856
	ds_write_b16 v71, v27 offset:46128
	ds_write_b16 v71, v28 offset:47488
	ds_write_b16 v71, v29 offset:47760
	ds_write_b16 v71, v30 offset:48032
	ds_write_b16 v71, v31 offset:48304
	ds_write_b16 v71, v0 offset:49664
	ds_write_b16 v71, v1 offset:49936
	ds_write_b16 v71, v2 offset:50208
	ds_write_b16 v71, v3 offset:50480
	ds_write_b16 v71, v4 offset:51840
	ds_write_b16 v71, v5 offset:52112
	ds_write_b16 v71, v6 offset:52384
	ds_write_b16 v71, v7 offset:52656
	ds_write_b16 v71, v8 offset:54016
	ds_write_b16 v71, v9 offset:54288
	ds_write_b16 v71, v10 offset:54560
	ds_write_b16 v71, v11 offset:54832
	ds_write_b16 v71, v12 offset:56192
	ds_write_b16 v71, v13 offset:56464
	ds_write_b16 v71, v14 offset:56736
	ds_write_b16 v71, v15 offset:57008
	s_waitcnt lgkmcnt(0)
	s_barrier
	ds_read_b128 v[36:39], v91 offset:40960
	ds_read_b128 v[50:53], v91 offset:40976
	ds_read_b128 v[54:57], v91 offset:40992
	ds_read_b128 v[26:29], v91 offset:41008
	global_load_dwordx4 v[12:15], v[102:103], off offset:2048
	global_load_dwordx4 v[0:3], v[100:101], off offset:48
	global_load_dwordx4 v[4:7], v[100:101], off offset:32
	global_load_dwordx4 v[8:11], v[100:101], off offset:16
	s_nop 1
	v_mov_b32_e32 v16, v216
	v_mov_b32_e32 v17, v217
	v_mov_b32_e32 v18, v218
	v_mov_b32_e32 v19, v219
	s_nop 1
	v_mov_b32_e32 v20, v212
	v_mov_b32_e32 v21, v213
	v_mov_b32_e32 v22, v214
	v_mov_b32_e32 v23, v215
	s_waitcnt lgkmcnt(3)
	v_lshlrev_b32_e32 v46, 16, v37
	v_and_b32_e32 v47, 0xffff0000, v37
	v_lshlrev_b32_e32 v58, 16, v36
	v_and_b32_e32 v59, 0xffff0000, v36
	v_lshlrev_b32_e32 v40, 16, v38
	v_and_b32_e32 v41, 0xffff0000, v38
	v_pk_mul_f32 v[64:65], v[46:47], v[46:47]
	v_pk_mul_f32 v[66:67], v[58:59], v[58:59]
	v_lshlrev_b32_e32 v34, 16, v39
	v_and_b32_e32 v35, 0xffff0000, v39
	v_pk_mul_f32 v[62:63], v[40:41], v[40:41]
	v_add_f32_e32 v64, v64, v65
	v_add_f32_e32 v65, v66, v67
	s_waitcnt lgkmcnt(2)
	v_lshlrev_b32_e32 v38, 16, v53
	v_and_b32_e32 v39, 0xffff0000, v53
	v_lshlrev_b32_e32 v42, 16, v52
	v_and_b32_e32 v43, 0xffff0000, v52
	v_lshlrev_b32_e32 v52, 16, v50
	v_and_b32_e32 v53, 0xffff0000, v50
	v_pk_mul_f32 v[60:61], v[34:35], v[34:35]
	v_add_f32_e32 v66, v62, v63
	v_add_f32_e32 v64, v65, v64
	v_lshlrev_b32_e32 v48, 16, v51
	v_and_b32_e32 v49, 0xffff0000, v51
	v_pk_mul_f32 v[92:93], v[52:53], v[52:53]
	v_add_f32_e32 v71, v60, v61
	v_add_f32_e32 v64, v66, v64
	v_pk_mul_f32 v[86:87], v[48:49], v[48:49]
	v_add_f32_e32 v67, v92, v93
	v_add_f32_e32 v64, v71, v64
	s_waitcnt lgkmcnt(1)
; DI unsigned pk2(float lo, float hi) { f32x2 v = {lo, hi}; bf16x2_t b = __builtin_convertvector(v, bf16x2_t); return __builtin_bit_cast(unsigned, b); }
; DI float bflo(unsigned u) { return __uint_as_float(u << 16); }
; DI float bfhi(unsigned u) { return __uint_as_float(u & 0xffff0000u); }
; DI float sigmoidf_(float x) { return __builtin_amdgcn_rcpf(1.f + __expf(-x)); }
; DI void gdn_out_unit(const Params& p, int U, char* lds) {
;     ...
;     for (int q = 0; q < 4; ++q) { const u32x4 w = *(const u32x4*)(ol + row * 136 + 32 * q4 + 8 * q);
; #pragma unroll
;       for (int e = 0; e < 4; ++e) { const float a0 = bflo(w[e]), a1 = bfhi(w[e]); ss += a0 * a0 + a1 * a1; } }
;     ss += __uint_as_float((unsigned)__builtin_amdgcn_update_dpp(0, (int)__float_as_uint(ss), 0xB1, 0xF, 0xF, true));
;     ss += __uint_as_float((unsigned)__builtin_amdgcn_update_dpp(0, (int)__float_as_uint(ss), 0x4E, 0xF, 0xF, true));
;     const float rstd = rsqrtf(ss * (1.f / 128.f) + 1e-6f);
; #pragma unroll
;     for (int q = 0; q < 4; ++q) {
;       const u32x4 w = *(const u32x4*)(ol + row * 136 + 32 * q4 + 8 * q), gz = *(const u32x4*)(gzp + 8 * q);
;       const f32x4 n0 = *(const f32x4*)(p.gdn_norm_w + 32 * q4 + 8 * q), n1 = *(const f32x4*)(p.gdn_norm_w + 32 * q4 + 8 * q + 4);
;       float y[8];
; #pragma unroll
;       for (int e = 0; e < 4; ++e) { const float z0 = bflo(gz[e]), z1 = bfhi(gz[e]);
;         const float g0 = (2 * e < 4) ? n0[(2 * e) & 3] : n1[(2 * e) & 3], g1 = (2 * e + 1 < 4) ? n0[(2 * e + 1) & 3] : n1[(2 * e + 1) & 3];
;         y[2 * e] = bflo(w[e]) * rstd * g0 * (z0 * sigmoidf_(z0));
;         y[2 * e + 1] = bfhi(w[e]) * rstd * g1 * (z1 * sigmoidf_(z1)); }
;       u32x4 wv4 = {pk2(y[0], y[1]), pk2(y[2], y[3]), pk2(y[4], y[5]), pk2(y[6], y[7])};
;       *(u32x4*)(op + 8 * q) = wv4;
;     }
	v_lshlrev_b32_e32 v36, 16, v57
	v_and_b32_e32 v37, 0xffff0000, v57
	v_and_b32_e32 v51, 0xffff0000, v55
	v_and_b32_e32 v57, 0xffff0000, v54
	v_pk_mul_f32 v[74:75], v[42:43], v[42:43]
	v_add_f32_e32 v84, v86, v87
	v_add_f32_e32 v64, v67, v64
	v_lshlrev_b32_e32 v44, 16, v56
	v_and_b32_e32 v45, 0xffff0000, v56
	v_lshlrev_b32_e32 v50, 16, v55
	v_lshlrev_b32_e32 v56, 16, v54
	v_pk_mul_f32 v[72:73], v[38:39], v[38:39]
	v_mov_b32_e32 v100, v51
	v_mov_b32_e32 v101, v57
	v_add_f32_e32 v74, v74, v75
	v_add_f32_e32 v64, v84, v64
	v_mov_b32_e32 v98, v50
	v_mov_b32_e32 v99, v56
	v_pk_mul_f32 v[100:101], v[100:101], v[100:101]
	v_add_f32_e32 v72, v72, v73
	v_add_f32_e32 v64, v74, v64
	v_mov_b32_e32 v96, v37
	v_mov_b32_e32 v97, v45
	v_pk_fma_f32 v[62:63], v[98:99], v[98:99], v[100:101]
	v_add_f32_e32 v64, v72, v64
	v_mov_b32_e32 v94, v36
	v_mov_b32_e32 v95, v44
	v_pk_mul_f32 v[96:97], v[96:97], v[96:97]
	v_add_f32_e32 v63, v63, v64
	s_waitcnt lgkmcnt(0)
	v_lshlrev_b32_e32 v25, 16, v27
	v_lshlrev_b32_e32 v24, 16, v26
	v_and_b32_e32 v27, 0xffff0000, v27
	v_and_b32_e32 v26, 0xffff0000, v26
	v_pk_fma_f32 v[60:61], v[94:95], v[94:95], v[96:97]
	v_add_f32_e32 v62, v62, v63
	v_pk_mul_f32 v[32:33], v[26:27], v[26:27]
	v_add_f32_e32 v61, v61, v62
	v_lshlrev_b32_e32 v31, 16, v29
	v_lshlrev_b32_e32 v30, 16, v28
	v_and_b32_e32 v29, 0xffff0000, v29
	v_and_b32_e32 v28, 0xffff0000, v28
	v_pk_fma_f32 v[32:33], v[24:25], v[24:25], v[32:33]
	v_add_f32_e32 v60, v60, v61
	v_pk_mul_f32 v[54:55], v[28:29], v[28:29]
	v_add_f32_e32 v32, v32, v60
	v_pk_fma_f32 v[54:55], v[30:31], v[30:31], v[54:55]
	v_add_f32_e32 v32, v33, v32
	v_add_f32_e32 v32, v54, v32
	v_add_f32_e32 v32, v55, v32
	s_waitcnt vmcnt(3)
	v_lshlrev_b32_e32 v60, 16, v13
	v_and_b32_e32 v61, 0xffff0000, v13
	v_add_f32_dpp v32, v32, v32 quad_perm:[1,0,3,2] row_mask:0xf bank_mask:0xf bound_ctrl:1
	v_lshlrev_b32_e32 v62, 16, v12
	v_and_b32_e32 v63, 0xffff0000, v12
	v_add_f32_dpp v32, v32, v32 quad_perm:[2,3,0,1] row_mask:0xf bank_mask:0xf bound_ctrl:1
	v_fmamk_f32 v32, v32, 0x3c000000, v89
	v_mul_f32_e32 v33, 0x4b800000, v32
	v_cmp_gt_f32_e32 vcc, s45, v32
	v_lshlrev_b32_e32 v12, 16, v15
	v_and_b32_e32 v13, 0xffff0000, v15
	v_cndmask_b32_e32 v32, v32, v33, vcc
	v_rsq_f32_e32 v32, v32
	s_nop 0
	v_mul_f32_e32 v33, 0x45800000, v32
	v_cndmask_b32_e32 v32, v32, v33, vcc
	v_pk_mul_f32 v[54:55], v[32:33], v[58:59] op_sel_hi:[0,1]
	v_pk_mul_f32 v[46:47], v[32:33], v[46:47] op_sel_hi:[0,1]
	v_pk_mul_f32 v[40:41], v[32:33], v[40:41] op_sel_hi:[0,1]
	v_pk_mul_f32 v[34:35], v[32:33], v[34:35] op_sel_hi:[0,1]
	v_lshlrev_b32_e32 v58, 16, v14
	v_and_b32_e32 v59, 0xffff0000, v14
	s_waitcnt vmcnt(0)
	v_pk_mul_f32 v[14:15], v[20:21], v[54:55]
	v_pk_mul_f32 v[20:21], v[22:23], v[46:47]
	v_pk_mul_f32 v[16:17], v[16:17], v[40:41]
	v_pk_mul_f32 v[18:19], v[18:19], v[34:35]
	v_mul_f32_e32 v22, 0xbfb8aa3b, v58
	v_mul_f32_e32 v23, 0xbfb8aa3b, v59
	v_mul_f32_e32 v33, 0xbfb8aa3b, v60
	v_mul_f32_e32 v34, 0xbfb8aa3b, v61
	v_mul_f32_e32 v35, 0xbfb8aa3b, v62
	v_mul_f32_e32 v40, 0xbfb8aa3b, v63
	v_mul_f32_e32 v41, 0xbfb8aa3b, v12
	v_mul_f32_e32 v46, 0xbfb8aa3b, v13
	v_exp_f32_e32 v22, v22
	v_exp_f32_e32 v23, v23
	v_exp_f32_e32 v33, v33
	v_exp_f32_e32 v34, v34
	v_exp_f32_e32 v35, v35
	v_exp_f32_e32 v40, v40
	v_exp_f32_e32 v41, v41
	v_exp_f32_e32 v46, v46
	v_add_f32_e32 v22, 1.0, v22
	v_add_f32_e32 v23, 1.0, v23
	v_add_f32_e32 v33, 1.0, v33
	v_add_f32_e32 v47, 1.0, v34
	v_add_f32_e32 v54, 1.0, v35
	v_add_f32_e32 v55, 1.0, v40
	v_add_f32_e32 v64, 1.0, v41
	v_add_f32_e32 v65, 1.0, v46
	v_rcp_f32_e32 v22, v22
	v_rcp_f32_e32 v23, v23
	v_rcp_f32_e32 v34, v33
	v_rcp_f32_e32 v35, v47
	v_rcp_f32_e32 v40, v54
	v_rcp_f32_e32 v41, v55
	v_rcp_f32_e32 v46, v64
	v_rcp_f32_e32 v47, v65
	v_pk_mul_f32 v[22:23], v[22:23], v[58:59]
	v_pk_mul_f32 v[34:35], v[34:35], v[60:61]
	v_pk_mul_f32 v[40:41], v[40:41], v[62:63]
	v_pk_mul_f32 v[12:13], v[46:47], v[12:13]
	v_pk_mul_f32 v[14:15], v[40:41], v[14:15]
	v_pk_mul_f32 v[20:21], v[34:35], v[20:21]
	v_pk_mul_f32 v[16:17], v[22:23], v[16:17]
	v_pk_mul_f32 v[18:19], v[12:13], v[18:19]
	v_cvt_pk_bf16_f32 v12, v14, v15
	v_cvt_pk_bf16_f32 v13, v20, v21
	v_cvt_pk_bf16_f32 v14, v16, v17
	v_cvt_pk_bf16_f32 v15, v18, v19
	global_store_dwordx4 v[68:69], v[12:15], off offset:3072
	s_nop 1
	v_mov_b32_e32 v12, v220
	v_mov_b32_e32 v13, v221
	v_mov_b32_e32 v14, v222
	v_mov_b32_e32 v15, v223
	s_nop 0
	s_nop 1
	v_mov_b32_e32 v16, v224
	v_mov_b32_e32 v17, v225
	v_mov_b32_e32 v18, v226
	v_mov_b32_e32 v19, v227
	v_pk_mul_f32 v[34:35], v[32:33], v[42:43] op_sel_hi:[0,1]
	v_lshlrev_b32_e32 v40, 16, v10
	v_and_b32_e32 v41, 0xffff0000, v10
	v_lshlrev_b32_e32 v42, 16, v9
	v_and_b32_e32 v43, 0xffff0000, v9
	v_lshlrev_b32_e32 v46, 16, v8
	v_and_b32_e32 v47, 0xffff0000, v8
	v_lshlrev_b32_e32 v8, 16, v11
	v_and_b32_e32 v9, 0xffff0000, v11
	v_pk_mul_f32 v[20:21], v[32:33], v[52:53] op_sel_hi:[0,1]
	v_pk_mul_f32 v[22:23], v[32:33], v[48:49] op_sel_hi:[0,1]
	v_pk_mul_f32 v[38:39], v[32:33], v[38:39] op_sel_hi:[0,1]
	v_mul_f32_e32 v10, 0xbfb8aa3b, v40
	v_mul_f32_e32 v11, 0xbfb8aa3b, v41
	v_mul_f32_e32 v33, 0xbfb8aa3b, v42
	v_mul_f32_e32 v48, 0xbfb8aa3b, v43
	v_mul_f32_e32 v49, 0xbfb8aa3b, v46
	v_mul_f32_e32 v52, 0xbfb8aa3b, v47
	v_mul_f32_e32 v53, 0xbfb8aa3b, v8
	v_mul_f32_e32 v54, 0xbfb8aa3b, v9
	v_exp_f32_e32 v10, v10
	v_exp_f32_e32 v11, v11
	v_exp_f32_e32 v33, v33
	v_exp_f32_e32 v48, v48
	v_exp_f32_e32 v49, v49
	v_exp_f32_e32 v52, v52
	v_exp_f32_e32 v53, v53
	v_exp_f32_e32 v54, v54
	v_add_f32_e32 v10, 1.0, v10
	v_add_f32_e32 v11, 1.0, v11
	v_add_f32_e32 v33, 1.0, v33
	v_add_f32_e32 v55, 1.0, v48
	v_add_f32_e32 v58, 1.0, v49
	v_add_f32_e32 v59, 1.0, v52
; DI unsigned pk2(float lo, float hi) { f32x2 v = {lo, hi}; bf16x2_t b = __builtin_convertvector(v, bf16x2_t); return __builtin_bit_cast(unsigned, b); }
; DI float bflo(unsigned u) { return __uint_as_float(u << 16); }
; DI float bfhi(unsigned u) { return __uint_as_float(u & 0xffff0000u); }
; DI float sigmoidf_(float x) { return __builtin_amdgcn_rcpf(1.f + __expf(-x)); }
; DI void gdn_out_unit(const Params& p, int U, char* lds) {
;     ...
;     for (int q = 0; q < 4; ++q) {
;       const u32x4 w = *(const u32x4*)(ol + row * 136 + 32 * q4 + 8 * q), gz = *(const u32x4*)(gzp + 8 * q);
;       const f32x4 n0 = *(const f32x4*)(p.gdn_norm_w + 32 * q4 + 8 * q), n1 = *(const f32x4*)(p.gdn_norm_w + 32 * q4 + 8 * q + 4);
;       float y[8];
; #pragma unroll
;       for (int e = 0; e < 4; ++e) { const float z0 = bflo(gz[e]), z1 = bfhi(gz[e]);
;         const float g0 = (2 * e < 4) ? n0[(2 * e) & 3] : n1[(2 * e) & 3], g1 = (2 * e + 1 < 4) ? n0[(2 * e + 1) & 3] : n1[(2 * e + 1) & 3];
;         y[2 * e] = bflo(w[e]) * rstd * g0 * (z0 * sigmoidf_(z0));
;         y[2 * e + 1] = bfhi(w[e]) * rstd * g1 * (z1 * sigmoidf_(z1)); }
;       u32x4 wv4 = {pk2(y[0], y[1]), pk2(y[2], y[3]), pk2(y[4], y[5]), pk2(y[6], y[7])};
;       *(u32x4*)(op + 8 * q) = wv4;
;     }
	v_add_f32_e32 v60, 1.0, v53
	v_add_f32_e32 v61, 1.0, v54
	v_rcp_f32_e32 v10, v10
	v_rcp_f32_e32 v11, v11
	v_rcp_f32_e32 v48, v33
	v_rcp_f32_e32 v49, v55
	v_rcp_f32_e32 v52, v58
	v_rcp_f32_e32 v53, v59
	v_rcp_f32_e32 v54, v60
	v_rcp_f32_e32 v55, v61
	v_pk_mul_f32 v[10:11], v[10:11], v[40:41]
	v_pk_mul_f32 v[40:41], v[48:49], v[42:43]
	v_pk_mul_f32 v[42:43], v[52:53], v[46:47]
	v_pk_mul_f32 v[8:9], v[54:55], v[8:9]
	v_cmp_lt_i32_e32 vcc, s48, v90
	s_or_b64 s[10:11], vcc, s[10:11]
	v_pk_mul_f32 v[12:13], v[12:13], v[20:21]
	v_pk_mul_f32 v[14:15], v[14:15], v[22:23]
	v_pk_mul_f32 v[16:17], v[16:17], v[34:35]
	v_pk_mul_f32 v[18:19], v[18:19], v[38:39]
	v_pk_mul_f32 v[12:13], v[42:43], v[12:13]
	v_pk_mul_f32 v[14:15], v[40:41], v[14:15]
	v_pk_mul_f32 v[10:11], v[10:11], v[16:17]
	v_pk_mul_f32 v[16:17], v[8:9], v[18:19]
	v_cvt_pk_bf16_f32 v8, v12, v13
	v_cvt_pk_bf16_f32 v9, v14, v15
	v_cvt_pk_bf16_f32 v10, v10, v11
	v_cvt_pk_bf16_f32 v11, v16, v17
	global_store_dwordx4 v[68:69], v[8:11], off offset:3088
	s_nop 1
	v_mov_b32_e32 v8, v228
	v_mov_b32_e32 v9, v229
	v_mov_b32_e32 v10, v230
	v_mov_b32_e32 v11, v231
	s_nop 0
	s_nop 1
	v_mov_b32_e32 v12, v232
	v_mov_b32_e32 v13, v233
	v_mov_b32_e32 v14, v234
	v_mov_b32_e32 v15, v235
	v_pk_mul_f32 v[22:23], v[32:33], v[36:37] op_sel_hi:[0,1]
	v_lshlrev_b32_e32 v34, 16, v6
	v_and_b32_e32 v35, 0xffff0000, v6
	v_lshlrev_b32_e32 v36, 16, v5
	v_and_b32_e32 v37, 0xffff0000, v5
	v_lshlrev_b32_e32 v38, 16, v4
	v_and_b32_e32 v39, 0xffff0000, v4
	v_lshlrev_b32_e32 v4, 16, v7
	v_and_b32_e32 v5, 0xffff0000, v7
	v_pk_mul_f32 v[16:17], v[32:33], v[56:57] op_sel_hi:[0,1]
	v_pk_mul_f32 v[18:19], v[32:33], v[50:51] op_sel_hi:[0,1]
	v_pk_mul_f32 v[20:21], v[32:33], v[44:45] op_sel_hi:[0,1]
	v_mul_f32_e32 v6, 0xbfb8aa3b, v34
	v_mul_f32_e32 v7, 0xbfb8aa3b, v35
	v_mul_f32_e32 v33, 0xbfb8aa3b, v36
	v_mul_f32_e32 v40, 0xbfb8aa3b, v37
	v_mul_f32_e32 v41, 0xbfb8aa3b, v38
	v_mul_f32_e32 v42, 0xbfb8aa3b, v39
	v_mul_f32_e32 v43, 0xbfb8aa3b, v4
	v_mul_f32_e32 v44, 0xbfb8aa3b, v5
	v_exp_f32_e32 v6, v6
	v_exp_f32_e32 v7, v7
	v_exp_f32_e32 v33, v33
	v_exp_f32_e32 v40, v40
	v_exp_f32_e32 v41, v41
	v_exp_f32_e32 v42, v42
	v_exp_f32_e32 v43, v43
	v_exp_f32_e32 v44, v44
	v_add_f32_e32 v6, 1.0, v6
	v_add_f32_e32 v7, 1.0, v7
	v_add_f32_e32 v33, 1.0, v33
	v_add_f32_e32 v45, 1.0, v40
	v_add_f32_e32 v46, 1.0, v41
	v_add_f32_e32 v47, 1.0, v42
	v_add_f32_e32 v48, 1.0, v43
	v_add_f32_e32 v49, 1.0, v44
	v_rcp_f32_e32 v6, v6
	v_rcp_f32_e32 v7, v7
	v_rcp_f32_e32 v40, v33
	v_rcp_f32_e32 v41, v45
	v_rcp_f32_e32 v42, v46
	v_rcp_f32_e32 v43, v47
	v_rcp_f32_e32 v44, v48
	v_rcp_f32_e32 v45, v49
	v_pk_mul_f32 v[6:7], v[6:7], v[34:35]
	v_pk_mul_f32 v[34:35], v[40:41], v[36:37]
	v_pk_mul_f32 v[36:37], v[42:43], v[38:39]
	v_pk_mul_f32 v[4:5], v[44:45], v[4:5]
	v_pk_mul_f32 v[8:9], v[8:9], v[16:17]
	v_pk_mul_f32 v[10:11], v[10:11], v[18:19]
	v_pk_mul_f32 v[12:13], v[12:13], v[20:21]
	v_pk_mul_f32 v[14:15], v[14:15], v[22:23]
	v_pk_mul_f32 v[8:9], v[36:37], v[8:9]
	v_pk_mul_f32 v[10:11], v[34:35], v[10:11]
	v_pk_mul_f32 v[6:7], v[6:7], v[12:13]
	v_pk_mul_f32 v[12:13], v[4:5], v[14:15]
	v_cvt_pk_bf16_f32 v4, v8, v9
	v_cvt_pk_bf16_f32 v5, v10, v11
	v_cvt_pk_bf16_f32 v6, v6, v7
	v_cvt_pk_bf16_f32 v7, v12, v13
	global_store_dwordx4 v[68:69], v[4:7], off offset:3104
	s_nop 1
	v_mov_b32_e32 v4, v240
	v_mov_b32_e32 v5, v241
	v_mov_b32_e32 v6, v242
	v_mov_b32_e32 v7, v243
	s_nop 0
	s_nop 1
	v_mov_b32_e32 v8, v236
	v_mov_b32_e32 v9, v237
	v_mov_b32_e32 v10, v238
	v_mov_b32_e32 v11, v239
	v_mov_b32_e32 v14, v25
	v_mov_b32_e32 v25, v26
	v_mov_b32_e32 v13, v28
	v_mov_b32_e32 v28, v31
	v_pk_mul_f32 v[16:17], v[32:33], v[24:25] op_sel_hi:[0,1]
	v_lshlrev_b32_e32 v20, 16, v2
	v_and_b32_e32 v21, 0xffff0000, v2
	v_lshlrev_b32_e32 v22, 16, v1
	v_and_b32_e32 v23, 0xffff0000, v1
	v_lshlrev_b32_e32 v24, 16, v0
	v_and_b32_e32 v25, 0xffff0000, v0
	v_lshlrev_b32_e32 v0, 16, v3
	v_and_b32_e32 v1, 0xffff0000, v3
	v_mov_b32_e32 v12, v30
	v_mov_b32_e32 v15, v27
	v_pk_mul_f32 v[18:19], v[32:33], v[28:29] op_sel_hi:[0,1]
	v_mul_f32_e32 v2, 0xbfb8aa3b, v21
	v_mul_f32_e32 v3, 0xbfb8aa3b, v20
	v_mul_f32_e32 v26, 0xbfb8aa3b, v23
	v_mul_f32_e32 v27, 0xbfb8aa3b, v22
	v_mul_f32_e32 v28, 0xbfb8aa3b, v25
	v_mul_f32_e32 v29, 0xbfb8aa3b, v24
	v_mul_f32_e32 v30, 0xbfb8aa3b, v0
	v_mul_f32_e32 v31, 0xbfb8aa3b, v1
	v_exp_f32_e32 v2, v2
	v_exp_f32_e32 v3, v3
	v_exp_f32_e32 v26, v26
	v_exp_f32_e32 v27, v27
	v_exp_f32_e32 v28, v28
	v_exp_f32_e32 v29, v29
	v_exp_f32_e32 v30, v30
	v_exp_f32_e32 v31, v31
	v_pk_mul_f32 v[12:13], v[32:33], v[12:13] op_sel_hi:[0,1]
	v_pk_mul_f32 v[14:15], v[32:33], v[14:15] op_sel_hi:[0,1]
	v_add_f32_e32 v2, 1.0, v2
	v_add_f32_e32 v32, 1.0, v3
	v_add_f32_e32 v26, 1.0, v26
	v_add_f32_e32 v33, 1.0, v27
	v_add_f32_e32 v28, 1.0, v28
	v_add_f32_e32 v34, 1.0, v29
	v_add_f32_e32 v30, 1.0, v30
	v_add_f32_e32 v31, 1.0, v31
	v_rcp_f32_e32 v3, v2
	v_rcp_f32_e32 v2, v32
	v_rcp_f32_e32 v27, v26
	v_rcp_f32_e32 v26, v33
	v_rcp_f32_e32 v29, v28
	v_rcp_f32_e32 v28, v34
	v_rcp_f32_e32 v30, v30
	v_rcp_f32_e32 v31, v31
	v_pk_mul_f32 v[2:3], v[2:3], v[20:21]
	v_pk_mul_f32 v[20:21], v[26:27], v[22:23]
	v_pk_mul_f32 v[22:23], v[28:29], v[24:25]
	v_pk_mul_f32 v[0:1], v[30:31], v[0:1]
	v_pk_mul_f32 v[4:5], v[4:5], v[12:13]
	v_pk_mul_f32 v[10:11], v[10:11], v[14:15]
	v_pk_mul_f32 v[8:9], v[8:9], v[16:17]
	v_pk_mul_f32 v[6:7], v[6:7], v[18:19]
	v_pk_mul_f32 v[2:3], v[2:3], v[4:5]
	v_pk_mul_f32 v[4:5], v[20:21], v[10:11]
	v_pk_mul_f32 v[8:9], v[22:23], v[8:9]
	v_pk_mul_f32 v[6:7], v[0:1], v[6:7]
	v_cvt_pk_bf16_f32 v0, v8, v9
	v_cvt_pk_bf16_f32 v1, v4, v5
	v_cvt_pk_bf16_f32 v2, v2, v3
	v_cvt_pk_bf16_f32 v3, v6, v7
	global_store_dwordx4 v[68:69], v[0:3], off offset:3120
	s_andn2_b64 exec, exec, s[10:11]
	s_cbranch_execnz .LBB0_1336
